# baseline (speedup 1.0000x reference)
.Lmy_noperm_in:
	s_cmp_gt_u32 s35, 0xff
	s_cbranch_scc1 .Lmy_prio_done
	s_setprio 1
